# P4b merge epilogue: first half of row group 6 also kept on chip (2 VGPRs + 4 KB spare LDS)
# speedup vs baseline: 1.0427x; 1.0027x over previous
.LBB0_826:
	v_add_f32_e32 v94, v94, v14
	v_add_f32_e32 v95, v95, v15
	v_mul_f32_e32 v94, 0xbfb8aa3b, v94
	v_mul_f32_e32 v95, 0xbfb8aa3b, v95
	v_exp_f32_e32 v94, v94
	v_exp_f32_e32 v95, v95
	s_waitcnt vmcnt(5)
	v_lshlrev_b32_e32 v108, 16, v30
	v_and_b32_e32 v109, 0xffff0000, v30
	v_add_f32_e32 v30, v96, v16
	v_mul_f32_e32 v30, 0xbfb8aa3b, v30
	v_add_f32_e32 v96, v97, v17
	v_add_f32_e32 v94, 1.0, v94
	v_add_f32_e32 v95, 1.0, v95
	v_exp_f32_e32 v30, v30
	v_mul_f32_e32 v96, 0xbfb8aa3b, v96
	v_rcp_f32_e32 v94, v94
	v_rcp_f32_e32 v95, v95
	v_exp_f32_e32 v97, v96
	v_add_f32_e32 v90, v90, v10
	v_lshlrev_b32_e32 v110, 16, v124
	v_and_b32_e32 v111, 0xffff0000, v124
	v_add_f32_e32 v30, 1.0, v30
	v_mul_f32_e32 v90, 0xbfb8aa3b, v90
	v_pk_fma_f32 v[94:95], v[94:95], v[108:109], v[110:111]
	v_rcp_f32_e32 v96, v30
	v_add_f32_e32 v30, 1.0, v97
	v_exp_f32_e32 v110, v90
	v_add_f32_e32 v90, v91, v11
	v_rcp_f32_e32 v97, v30
	v_mul_f32_e32 v90, 0xbfb8aa3b, v90
	v_exp_f32_e32 v111, v90
	v_lshlrev_b32_e32 v30, 16, v31
	v_and_b32_e32 v31, 0xffff0000, v31
	v_lshlrev_b32_e32 v108, 16, v125
	v_and_b32_e32 v109, 0xffff0000, v125
	v_pk_fma_f32 v[90:91], v[96:97], v[30:31], v[108:109]
	v_lshlrev_b32_e32 v96, 16, v32
	v_and_b32_e32 v97, 0xffff0000, v32
	v_add_f32_e32 v32, v92, v12
	v_add_f32_e32 v92, v93, v13
	v_add_f32_e32 v30, 1.0, v110
	v_add_f32_e32 v31, 1.0, v111
	v_mul_f32_e32 v32, 0xbfb8aa3b, v32
	v_mul_f32_e32 v92, 0xbfb8aa3b, v92
	v_rcp_f32_e32 v30, v30
	v_rcp_f32_e32 v31, v31
	v_exp_f32_e32 v32, v32
	v_exp_f32_e32 v110, v92
	v_lshlrev_b32_e32 v108, 16, v122
	v_and_b32_e32 v109, 0xffff0000, v122
	v_pk_fma_f32 v[92:93], v[30:31], v[96:97], v[108:109]
	v_add_f32_e32 v30, 1.0, v32
	v_add_f32_e32 v31, 1.0, v110
	v_rcp_f32_e32 v30, v30
	v_rcp_f32_e32 v31, v31
	v_add_f32_e32 v86, v86, v6
	v_add_f32_e32 v87, v87, v7
	v_lshlrev_b32_e32 v32, 16, v33
	v_and_b32_e32 v33, 0xffff0000, v33
	v_lshlrev_b32_e32 v96, 16, v123
	v_and_b32_e32 v97, 0xffff0000, v123
	v_mul_f32_e32 v86, 0xbfb8aa3b, v86
	v_mul_f32_e32 v87, 0xbfb8aa3b, v87
	v_pk_fma_f32 v[96:97], v[30:31], v[32:33], v[96:97]
	v_exp_f32_e32 v86, v86
	v_exp_f32_e32 v87, v87
	v_cvt_pk_bf16_f32 v30, v94, v95
	v_cvt_pk_bf16_f32 v31, v90, v91
	v_cvt_pk_bf16_f32 v32, v92, v93
	v_cvt_pk_bf16_f32 v33, v96, v97
	v_lshl_add_u64 v[90:91], v[120:121], 0, v[0:1]
	v_mov_b32_e32 v214, v30
	v_mov_b32_e32 v215, v31
	v_mov_b32_e32 v220, v32
	v_mov_b32_e32 v221, v33
	s_mov_b64 exec, s[34:35]
	global_store_dwordx4 v[90:91], v[30:33], off
	s_mov_b64 exec, -1
	v_add_f32_e32 v82, v82, v2
	v_add_f32_e32 v83, v83, v3
	s_waitcnt vmcnt(5)
	v_lshlrev_b32_e32 v32, 16, v22
	v_and_b32_e32 v33, 0xffff0000, v22
	v_add_f32_e32 v22, v88, v8
	v_mul_f32_e32 v22, 0xbfb8aa3b, v22
	v_add_f32_e32 v88, v89, v9
	v_add_f32_e32 v30, 1.0, v86
	v_add_f32_e32 v31, 1.0, v87
	v_exp_f32_e32 v22, v22
	v_mul_f32_e32 v88, 0xbfb8aa3b, v88
	v_rcp_f32_e32 v30, v30
	v_rcp_f32_e32 v31, v31
	v_exp_f32_e32 v88, v88
	v_lshlrev_b32_e32 v86, 16, v118
	v_and_b32_e32 v87, 0xffff0000, v118
	v_add_f32_e32 v22, 1.0, v22
	v_pk_fma_f32 v[30:31], v[30:31], v[32:33], v[86:87]
	v_rcp_f32_e32 v32, v22
	v_add_f32_e32 v22, 1.0, v88
	v_mul_f32_e32 v82, 0xbfb8aa3b, v82
	v_mul_f32_e32 v83, 0xbfb8aa3b, v83
	v_rcp_f32_e32 v33, v22
	v_exp_f32_e32 v82, v82
	v_exp_f32_e32 v83, v83
	v_lshlrev_b32_e32 v22, 16, v23
	v_and_b32_e32 v23, 0xffff0000, v23
	v_lshlrev_b32_e32 v86, 16, v119
	v_and_b32_e32 v87, 0xffff0000, v119
	v_pk_fma_f32 v[32:33], v[32:33], v[22:23], v[86:87]
	v_add_f32_e32 v22, 1.0, v82
	v_add_f32_e32 v23, 1.0, v83
	v_lshlrev_b32_e32 v82, 16, v24
	v_and_b32_e32 v83, 0xffff0000, v24
	v_add_f32_e32 v24, v84, v4
	v_add_f32_e32 v84, v85, v5
	v_mul_f32_e32 v24, 0xbfb8aa3b, v24
	v_mul_f32_e32 v84, 0xbfb8aa3b, v84
	v_rcp_f32_e32 v22, v22
	v_rcp_f32_e32 v23, v23
	v_exp_f32_e32 v24, v24
	v_exp_f32_e32 v84, v84
	v_lshlrev_b32_e32 v86, 16, v116
	v_and_b32_e32 v87, 0xffff0000, v116
	v_pk_fma_f32 v[82:83], v[22:23], v[82:83], v[86:87]
	v_add_f32_e32 v22, 1.0, v24
	v_add_f32_e32 v23, 1.0, v84
	v_rcp_f32_e32 v22, v22
	v_rcp_f32_e32 v23, v23
	v_lshlrev_b32_e32 v24, 16, v25
	v_and_b32_e32 v25, 0xffff0000, v25
	v_lshlrev_b32_e32 v84, 16, v117
	v_and_b32_e32 v85, 0xffff0000, v117
	v_pk_fma_f32 v[84:85], v[22:23], v[24:25], v[84:85]
	v_cvt_pk_bf16_f32 v22, v30, v31
	v_cvt_pk_bf16_f32 v23, v32, v33
	v_cvt_pk_bf16_f32 v24, v82, v83
	v_cvt_pk_bf16_f32 v25, v84, v85
	ds_write_b128 v222, v[22:25]
	s_mov_b64 exec, s[34:35]
	global_store_dwordx4 v[90:91], v[22:25], off offset:256
	s_mov_b64 exec, -1
	v_mov_b32_e32 v84, 0
	s_and_b64 vcc, exec, s[0:1]
	v_or_b32_e32 v24, 32, v114
	v_mov_b64_e32 v[22:23], s[12:13]
	v_mad_i64_i32 v[22:23], s[28:29], v24, s66, v[22:23]
	v_lshl_add_u64 v[22:23], s[26:27], 1, v[22:23]
	v_lshl_add_u64 v[22:23], v[22:23], 0, v[0:1]
	global_load_dwordx4 v[30:33], v[22:23], off
	v_ashrrev_i32_e32 v25, 31, v24
	v_lshlrev_b64 v[24:25], 11, v[24:25]
	v_lshl_add_u64 v[86:87], s[10:11], 0, v[24:25]
	v_mov_b32_e32 v90, 0
	v_mov_b32_e32 v91, 0
	v_mov_b32_e32 v88, 0
	v_mov_b32_e32 v89, 0
	s_cbranch_vccnz .LBB0_828
	v_lshl_add_u64 v[24:25], v[86:87], 0, v[0:1]
	v_lshrrev_b32_e32 v90, 1, v222
	v_add_u32_e32 v90, 0x12060, v90
	ds_read_b64 v[90:91], v90
	s_waitcnt lgkmcnt(0)
	v_mov_b32_e32 v88, v223
	v_mov_b32_e32 v89, v250

.LBB0_834:
	v_add_f32_e32 v62, v62, v14
	v_add_f32_e32 v63, v63, v15
	v_mul_f32_e32 v62, 0xbfb8aa3b, v62
	v_mul_f32_e32 v63, 0xbfb8aa3b, v63
	v_exp_f32_e32 v62, v62
	v_exp_f32_e32 v63, v63
	s_waitcnt vmcnt(5)
	v_lshlrev_b32_e32 v76, 16, v30
	v_and_b32_e32 v77, 0xffff0000, v30
	v_add_f32_e32 v30, v64, v16
	v_mul_f32_e32 v30, 0xbfb8aa3b, v30
	v_add_f32_e32 v64, v65, v17
	v_add_f32_e32 v62, 1.0, v62
	v_add_f32_e32 v63, 1.0, v63
	v_exp_f32_e32 v30, v30
	v_mul_f32_e32 v64, 0xbfb8aa3b, v64
	v_rcp_f32_e32 v62, v62
	v_rcp_f32_e32 v63, v63
	v_exp_f32_e32 v65, v64
	v_add_f32_e32 v58, v58, v10
	v_lshlrev_b32_e32 v78, 16, v90
	v_and_b32_e32 v79, 0xffff0000, v90
	v_add_f32_e32 v30, 1.0, v30
	v_mul_f32_e32 v58, 0xbfb8aa3b, v58
	v_pk_fma_f32 v[62:63], v[62:63], v[76:77], v[78:79]
	v_rcp_f32_e32 v64, v30
	v_add_f32_e32 v30, 1.0, v65
	v_exp_f32_e32 v78, v58
	v_add_f32_e32 v58, v59, v11
	v_rcp_f32_e32 v65, v30
	v_mul_f32_e32 v58, 0xbfb8aa3b, v58
	v_exp_f32_e32 v79, v58
	v_lshlrev_b32_e32 v30, 16, v31
	v_and_b32_e32 v31, 0xffff0000, v31
	v_lshlrev_b32_e32 v76, 16, v91
	v_and_b32_e32 v77, 0xffff0000, v91
	v_pk_fma_f32 v[58:59], v[64:65], v[30:31], v[76:77]
	v_lshlrev_b32_e32 v64, 16, v32
	v_and_b32_e32 v65, 0xffff0000, v32
	v_add_f32_e32 v32, v60, v12
	v_add_f32_e32 v60, v61, v13
	v_add_f32_e32 v30, 1.0, v78
	v_add_f32_e32 v31, 1.0, v79
	v_mul_f32_e32 v32, 0xbfb8aa3b, v32
	v_mul_f32_e32 v60, 0xbfb8aa3b, v60
	v_rcp_f32_e32 v30, v30
	v_rcp_f32_e32 v31, v31
	v_exp_f32_e32 v32, v32
	v_exp_f32_e32 v78, v60
	v_lshlrev_b32_e32 v76, 16, v88
	v_and_b32_e32 v77, 0xffff0000, v88
	v_pk_fma_f32 v[60:61], v[30:31], v[64:65], v[76:77]
	v_add_f32_e32 v30, 1.0, v32
	v_add_f32_e32 v31, 1.0, v78
	v_rcp_f32_e32 v30, v30
	v_rcp_f32_e32 v31, v31
	v_add_f32_e32 v54, v54, v6
	v_add_f32_e32 v55, v55, v7
	v_lshlrev_b32_e32 v32, 16, v33
	v_and_b32_e32 v33, 0xffff0000, v33
	v_lshlrev_b32_e32 v64, 16, v89
	v_and_b32_e32 v65, 0xffff0000, v89
	v_mul_f32_e32 v54, 0xbfb8aa3b, v54
	v_mul_f32_e32 v55, 0xbfb8aa3b, v55
	v_pk_fma_f32 v[64:65], v[30:31], v[32:33], v[64:65]
	v_exp_f32_e32 v54, v54
	v_exp_f32_e32 v55, v55
	v_cvt_pk_bf16_f32 v30, v62, v63
	v_cvt_pk_bf16_f32 v31, v58, v59
	v_cvt_pk_bf16_f32 v32, v60, v61
	v_cvt_pk_bf16_f32 v33, v64, v65
	v_lshl_add_u64 v[58:59], v[86:87], 0, v[0:1]
	v_mov_b32_e32 v223, v32
	v_mov_b32_e32 v250, v33
	s_mov_b64 exec, s[34:35]
	global_store_dwordx4 v[58:59], v[30:33], off
	s_mov_b64 exec, -1
	s_nop 0
	v_lshrrev_b32_e32 v33, 1, v222
	v_add_u32_e32 v33, 0x12060, v33
	ds_write_b64 v33, v[30:31]
	v_add_f32_e32 v50, v50, v2
	v_add_f32_e32 v51, v51, v3
	s_waitcnt vmcnt(5)
	v_lshlrev_b32_e32 v32, 16, v22
	v_and_b32_e32 v33, 0xffff0000, v22
	v_add_f32_e32 v22, v56, v8
	v_mul_f32_e32 v22, 0xbfb8aa3b, v22
	v_add_f32_e32 v56, v57, v9
	v_add_f32_e32 v30, 1.0, v54
	v_add_f32_e32 v31, 1.0, v55
	v_exp_f32_e32 v22, v22
	v_mul_f32_e32 v56, 0xbfb8aa3b, v56
	v_rcp_f32_e32 v30, v30
	v_rcp_f32_e32 v31, v31
	v_exp_f32_e32 v56, v56
	v_lshlrev_b32_e32 v54, 16, v84
	v_and_b32_e32 v55, 0xffff0000, v84
	v_add_f32_e32 v22, 1.0, v22
	v_pk_fma_f32 v[30:31], v[30:31], v[32:33], v[54:55]
	v_rcp_f32_e32 v32, v22
	v_add_f32_e32 v22, 1.0, v56
	v_mul_f32_e32 v50, 0xbfb8aa3b, v50
	v_mul_f32_e32 v51, 0xbfb8aa3b, v51
	v_rcp_f32_e32 v33, v22
	v_exp_f32_e32 v50, v50
	v_exp_f32_e32 v51, v51
	v_lshlrev_b32_e32 v22, 16, v23
	v_and_b32_e32 v23, 0xffff0000, v23
	v_lshlrev_b32_e32 v54, 16, v85
	v_and_b32_e32 v55, 0xffff0000, v85
	v_pk_fma_f32 v[32:33], v[32:33], v[22:23], v[54:55]
	v_add_f32_e32 v22, 1.0, v50
	v_add_f32_e32 v23, 1.0, v51
	v_lshlrev_b32_e32 v50, 16, v24
	v_and_b32_e32 v51, 0xffff0000, v24
	v_add_f32_e32 v24, v52, v4
	v_add_f32_e32 v52, v53, v5
	v_mul_f32_e32 v24, 0xbfb8aa3b, v24
	v_mul_f32_e32 v52, 0xbfb8aa3b, v52
	v_rcp_f32_e32 v22, v22
	v_rcp_f32_e32 v23, v23
	v_exp_f32_e32 v24, v24
	v_exp_f32_e32 v52, v52
	v_add_f32_e32 v14, v46, v14
	v_add_f32_e32 v15, v47, v15
	v_lshlrev_b32_e32 v54, 16, v82
	v_and_b32_e32 v55, 0xffff0000, v82
	v_mul_f32_e32 v14, 0xbfb8aa3b, v14
	v_mul_f32_e32 v15, 0xbfb8aa3b, v15
	v_pk_fma_f32 v[50:51], v[22:23], v[50:51], v[54:55]
	v_add_f32_e32 v22, 1.0, v24
	v_add_f32_e32 v23, 1.0, v52
	v_exp_f32_e32 v14, v14
	v_exp_f32_e32 v15, v15
	v_rcp_f32_e32 v22, v22
	v_rcp_f32_e32 v23, v23
	v_add_f32_e32 v16, v48, v16
	v_add_f32_e32 v17, v49, v17
	v_mul_f32_e32 v16, 0xbfb8aa3b, v16
	v_mul_f32_e32 v17, 0xbfb8aa3b, v17
	v_add_f32_e32 v10, v42, v10
	v_add_f32_e32 v11, v43, v11
	v_exp_f32_e32 v16, v16
	v_exp_f32_e32 v17, v17
	v_mul_f32_e32 v10, 0xbfb8aa3b, v10
	v_mul_f32_e32 v11, 0xbfb8aa3b, v11
	v_lshlrev_b32_e32 v24, 16, v25
	v_and_b32_e32 v25, 0xffff0000, v25
	v_lshlrev_b32_e32 v52, 16, v83
	v_and_b32_e32 v53, 0xffff0000, v83
	v_add_f32_e32 v14, 1.0, v14
	v_add_f32_e32 v15, 1.0, v15
	v_exp_f32_e32 v10, v10
	v_exp_f32_e32 v11, v11
	v_pk_fma_f32 v[52:53], v[22:23], v[24:25], v[52:53]
	v_rcp_f32_e32 v14, v14
	v_rcp_f32_e32 v15, v15
	v_add_f32_e32 v12, v44, v12
	v_cvt_pk_bf16_f32 v22, v30, v31
	v_cvt_pk_bf16_f32 v23, v32, v33
	v_cvt_pk_bf16_f32 v24, v50, v51
	v_cvt_pk_bf16_f32 v25, v52, v53
	v_mul_f32_e32 v12, 0xbfb8aa3b, v12
	global_store_dwordx4 v[58:59], v[22:25], off offset:256
	v_add_f32_e32 v16, 1.0, v16
	v_add_f32_e32 v17, 1.0, v17
	s_waitcnt vmcnt(3)
	v_lshlrev_b32_e32 v22, 16, v26
	v_and_b32_e32 v23, 0xffff0000, v26
	v_exp_f32_e32 v26, v12
	v_add_f32_e32 v12, v45, v13
	v_lshlrev_b32_e32 v24, 16, v74
	v_and_b32_e32 v25, 0xffff0000, v74
	v_rcp_f32_e32 v16, v16
	v_rcp_f32_e32 v17, v17
	v_add_f32_e32 v10, 1.0, v10
	v_add_f32_e32 v11, 1.0, v11
	v_mul_f32_e32 v12, 0xbfb8aa3b, v12
	v_pk_fma_f32 v[14:15], v[14:15], v[22:23], v[24:25]
	v_lshlrev_b32_e32 v22, 16, v27
	v_and_b32_e32 v23, 0xffff0000, v27
	v_rcp_f32_e32 v10, v10
	v_rcp_f32_e32 v11, v11
	v_exp_f32_e32 v27, v12
	v_lshlrev_b32_e32 v24, 16, v75
	v_and_b32_e32 v25, 0xffff0000, v75
	v_pk_fma_f32 v[16:17], v[16:17], v[22:23], v[24:25]
	v_lshlrev_b32_e32 v22, 16, v28
	v_and_b32_e32 v23, 0xffff0000, v28
	v_lshlrev_b32_e32 v24, 16, v72
	v_and_b32_e32 v25, 0xffff0000, v72
	v_pk_fma_f32 v[12:13], v[10:11], v[22:23], v[24:25]
	v_add_f32_e32 v10, 1.0, v26
	v_add_f32_e32 v11, 1.0, v27
	v_rcp_f32_e32 v10, v10
	v_rcp_f32_e32 v11, v11
	v_lshlrev_b32_e32 v22, 16, v29
	v_and_b32_e32 v23, 0xffff0000, v29
	v_lshlrev_b32_e32 v24, 16, v73
	v_and_b32_e32 v25, 0xffff0000, v73
	v_pk_fma_f32 v[22:23], v[10:11], v[22:23], v[24:25]
	v_cvt_pk_bf16_f32 v10, v14, v15
	v_lshl_add_u64 v[14:15], v[70:71], 0, v[0:1]
	v_add_f32_e32 v0, v38, v6
	v_mul_f32_e32 v0, 0xbfb8aa3b, v0
	v_add_f32_e32 v6, v39, v7
	v_exp_f32_e32 v0, v0
	v_mul_f32_e32 v6, 0xbfb8aa3b, v6
	v_exp_f32_e32 v7, v6
	v_cvt_pk_bf16_f32 v11, v16, v17
	v_add_f32_e32 v0, 1.0, v0
	v_rcp_f32_e32 v6, v0
	v_add_f32_e32 v0, 1.0, v7
	v_rcp_f32_e32 v7, v0
	v_add_f32_e32 v0, v40, v8
	v_mul_f32_e32 v0, 0xbfb8aa3b, v0
	v_add_f32_e32 v8, v41, v9
	v_exp_f32_e32 v0, v0
	v_mul_f32_e32 v8, 0xbfb8aa3b, v8
	v_exp_f32_e32 v9, v8
	v_cvt_pk_bf16_f32 v12, v12, v13
	v_add_f32_e32 v0, 1.0, v0
	v_rcp_f32_e32 v8, v0
	v_add_f32_e32 v0, 1.0, v9
	v_rcp_f32_e32 v9, v0
	v_add_f32_e32 v0, v34, v2
	v_mul_f32_e32 v0, 0xbfb8aa3b, v0
	v_add_f32_e32 v2, v35, v3
	v_exp_f32_e32 v0, v0
	v_mul_f32_e32 v2, 0xbfb8aa3b, v2
	v_exp_f32_e32 v3, v2
	v_cvt_pk_bf16_f32 v13, v22, v23
	v_add_f32_e32 v0, 1.0, v0
	v_rcp_f32_e32 v2, v0
	v_add_f32_e32 v0, 1.0, v3
	v_rcp_f32_e32 v3, v0
	v_add_f32_e32 v0, v36, v4
	v_mul_f32_e32 v0, 0xbfb8aa3b, v0
	v_add_f32_e32 v4, v37, v5
	v_exp_f32_e32 v0, v0
	v_mul_f32_e32 v4, 0xbfb8aa3b, v4
	v_exp_f32_e32 v16, v4
	global_store_dwordx4 v[14:15], v[10:13], off
	v_add_f32_e32 v0, 1.0, v0
	s_andn2_b64 vcc, exec, s[38:39]
	s_waitcnt vmcnt(3)
	v_lshlrev_b32_e32 v10, 16, v18
	v_and_b32_e32 v11, 0xffff0000, v18
	v_lshlrev_b32_e32 v12, 16, v68
	v_and_b32_e32 v13, 0xffff0000, v68
	v_pk_fma_f32 v[6:7], v[6:7], v[10:11], v[12:13]
	v_lshlrev_b32_e32 v10, 16, v19
	v_and_b32_e32 v11, 0xffff0000, v19
	v_lshlrev_b32_e32 v12, 16, v69
	v_and_b32_e32 v13, 0xffff0000, v69
	v_pk_fma_f32 v[8:9], v[8:9], v[10:11], v[12:13]
	v_lshlrev_b32_e32 v10, 16, v20
	v_and_b32_e32 v11, 0xffff0000, v20
	v_lshlrev_b32_e32 v12, 16, v66
	v_and_b32_e32 v13, 0xffff0000, v66
	v_pk_fma_f32 v[4:5], v[2:3], v[10:11], v[12:13]
	v_rcp_f32_e32 v2, v0
	v_add_f32_e32 v0, 1.0, v16
	v_rcp_f32_e32 v3, v0
	v_lshlrev_b32_e32 v10, 16, v21
	v_and_b32_e32 v11, 0xffff0000, v21
	v_lshlrev_b32_e32 v12, 16, v67
	v_and_b32_e32 v13, 0xffff0000, v67
	v_pk_fma_f32 v[10:11], v[2:3], v[10:11], v[12:13]
	v_cvt_pk_bf16_f32 v2, v6, v7
	v_cvt_pk_bf16_f32 v3, v8, v9
	v_cvt_pk_bf16_f32 v4, v4, v5
	v_cvt_pk_bf16_f32 v5, v10, v11
	s_mov_b64 s[0:1], -1
	global_store_dwordx4 v[14:15], v[2:5], off offset:256
	s_cbranch_vccnz .LBB0_795
	v_readlane_b32 s28, v253, 4
	v_readlane_b32 s30, v253, 6
	v_readlane_b32 s31, v253, 7
	v_readlane_b32 s29, v253, 5
	s_and_b64 vcc, exec, s[8:9]
	v_mov_b64_e32 v[36:37], s[30:31]
	v_mov_b64_e32 v[160:161], s[30:31]
	v_mov_b64_e32 v[156:157], s[30:31]
	v_mov_b64_e32 v[144:145], s[30:31]
	v_mov_b64_e32 v[140:141], s[30:31]
	v_mov_b64_e32 v[128:129], s[30:31]
	v_mov_b64_e32 v[124:125], s[30:31]
	v_mov_b64_e32 v[112:113], s[30:31]
	v_mov_b64_e32 v[108:109], s[30:31]
	v_mov_b64_e32 v[152:153], s[30:31]
	v_mov_b64_e32 v[148:149], s[30:31]
	v_mov_b64_e32 v[136:137], s[30:31]
	v_mov_b64_e32 v[132:133], s[30:31]
	v_mov_b64_e32 v[120:121], s[30:31]
	v_mov_b64_e32 v[116:117], s[30:31]
	v_mov_b64_e32 v[104:105], s[30:31]
	v_mov_b64_e32 v[100:101], s[30:31]
	v_mov_b64_e32 v[96:97], s[30:31]
	v_mov_b64_e32 v[92:93], s[30:31]
	v_mov_b64_e32 v[80:81], s[30:31]
	v_mov_b64_e32 v[76:77], s[30:31]
	v_mov_b64_e32 v[64:65], s[30:31]
	v_mov_b64_e32 v[60:61], s[30:31]
	v_mov_b64_e32 v[48:49], s[30:31]
	v_mov_b64_e32 v[44:45], s[30:31]
	v_mov_b64_e32 v[88:89], s[30:31]
	v_mov_b64_e32 v[84:85], s[30:31]
	v_mov_b64_e32 v[72:73], s[30:31]
	v_mov_b64_e32 v[68:69], s[30:31]
	v_mov_b64_e32 v[56:57], s[30:31]
	v_mov_b64_e32 v[52:53], s[30:31]
	v_mov_b64_e32 v[40:41], s[30:31]
	v_mov_b64_e32 v[34:35], s[28:29]
	v_mov_b64_e32 v[158:159], s[28:29]
	v_mov_b64_e32 v[154:155], s[28:29]
	v_mov_b64_e32 v[142:143], s[28:29]
	v_mov_b64_e32 v[138:139], s[28:29]
	v_mov_b64_e32 v[126:127], s[28:29]
	v_mov_b64_e32 v[122:123], s[28:29]
	v_mov_b64_e32 v[110:111], s[28:29]
	v_mov_b64_e32 v[106:107], s[28:29]
	v_mov_b64_e32 v[150:151], s[28:29]
	v_mov_b64_e32 v[146:147], s[28:29]
	v_mov_b64_e32 v[134:135], s[28:29]
	v_mov_b64_e32 v[130:131], s[28:29]
	v_mov_b64_e32 v[118:119], s[28:29]
	v_mov_b64_e32 v[114:115], s[28:29]
	v_mov_b64_e32 v[102:103], s[28:29]
	v_mov_b64_e32 v[98:99], s[28:29]
	v_mov_b64_e32 v[94:95], s[28:29]
	v_mov_b64_e32 v[90:91], s[28:29]
	v_mov_b64_e32 v[78:79], s[28:29]
	v_mov_b64_e32 v[74:75], s[28:29]
	v_mov_b64_e32 v[62:63], s[28:29]
	v_mov_b64_e32 v[58:59], s[28:29]
	v_mov_b64_e32 v[46:47], s[28:29]
	v_mov_b64_e32 v[42:43], s[28:29]
	v_mov_b64_e32 v[86:87], s[28:29]
	v_mov_b64_e32 v[82:83], s[28:29]
	v_mov_b64_e32 v[70:71], s[28:29]
	v_mov_b64_e32 v[66:67], s[28:29]
	v_mov_b64_e32 v[54:55], s[28:29]
	v_mov_b64_e32 v[50:51], s[28:29]
	v_mov_b64_e32 v[38:39], s[28:29]
	s_cbranch_vccz .LBB0_794
	s_barrier
	s_branch .LBB0_794

.LBB0_895:
	v_mov_b32_e32 v250, 0xd80
	v_mov_b32_e32 v211, 0x3727c5ac
	v_mov_b32_e32 v212, 0x260
	v_mov_b32_e32 v214, 0x1200
	v_mov_b32_e32 v215, 0xff800000
	v_mov_b32_e32 v220, 0x1680
	v_mov_b32_e32 v221, 0x1b00
	v_mov_b32_e32 v222, 0x1f80
	v_mov_b32_e32 v223, 0x40e00000
	v_readlane_b32 s0, v252, 61
	v_readlane_b32 s1, v252, 62
	s_xor_b64 s[2:3], s[0:1], -1
	s_cmp_le_i32 s90, s14
	s_cselect_b64 s[0:1], -1, 0
	s_and_b64 s[4:5], s[0:1], s[4:5]
	s_andn2_b64 vcc, exec, s[4:5]
	s_cbranch_vccnz .LBB0_922
	v_readlane_b32 s4, v252, 61
	v_readlane_b32 s5, v252, 62
	s_and_b64 s[4:5], s[4:5], exec
	s_mov_b64 s[6:7], s[84:85]
	s_load_dwordx2 s[4:5], s[6:7], 0x100
	s_cselect_b32 s8, 0, 0xf8
	s_add_u32 s8, s6, s8
	s_addc_u32 s9, s7, 0
	s_mov_b64 s[10:11], -1
	s_and_b64 vcc, exec, s[2:3]
	s_cbranch_vccz .LBB0_898
	s_waitcnt lgkmcnt(0)
	s_add_u32 s18, s4, 0x1e00000
	s_addc_u32 s19, s5, 0
	s_mov_b64 s[10:11], 0
